# sort1 conv x8 stores widened to 16B (DPP pair-combine) with sc1 write-through
# baseline (speedup 1.0000x reference)
.LBB0_15:
	s_andn2_b64 vcc, exec, s[4:5]
	s_cbranch_vccnz .LBB0_21
	s_sleep 85
	s_load_dwordx2 s[10:11], s[0:1], 0x0
	s_load_dwordx2 s[8:9], s[0:1], 0x60
	s_lshl_b32 s3, s2, 1
	s_add_i32 s12, s3, 0xfffffe00
	s_mov_b32 s13, 0
	v_lshlrev_b32_e32 v4, 3, v0
	s_lshl_b64 s[4:5], s[12:13], 13
	v_or_b32_e32 v2, s4, v4
	v_mov_b32_e32 v3, s5
	s_waitcnt lgkmcnt(0)
	v_lshl_add_u64 v[6:7], v[2:3], 2, s[10:11]
	global_load_dwordx4 v[12:15], v[6:7], off
	global_load_dwordx4 v[16:19], v[6:7], off offset:16
	v_mbcnt_lo_u32_b32 v1, -1, 0
	v_mbcnt_hi_u32_b32 v1, -1, v1
	v_and_b32_e32 v6, 64, v1
	v_xor_b32_e32 v5, 1, v1
	v_add_u32_e32 v9, 64, v6
	v_cmp_lt_i32_e32 vcc, v5, v9
	v_xor_b32_e32 v7, 2, v1
	v_xor_b32_e32 v20, 8, v1
	v_cndmask_b32_e32 v5, v1, v5, vcc
	v_lshlrev_b32_e32 v6, 2, v5
	v_cmp_lt_i32_e32 vcc, v7, v9
	v_and_b32_e32 v10, 15, v0
	v_cmp_eq_u32_e64 s[4:5], 0, v10
	v_cndmask_b32_e32 v7, v1, v7, vcc
	v_lshlrev_b32_e32 v7, 2, v7
	s_mov_b32 s3, 0x42fe0000
	s_waitcnt vmcnt(1)
	v_max3_f32 v5, |v12|, 0, |v13|
	v_max3_f32 v5, v5, |v14|, |v15|
	s_waitcnt vmcnt(0)
	v_max3_f32 v5, v5, |v16|, |v17|
	v_max3_f32 v5, v5, |v18|, |v19|
	ds_bpermute_b32 v8, v6, v5
	s_waitcnt lgkmcnt(0)
	v_max_f32_e32 v8, v8, v8
	v_max_f32_e32 v5, v5, v8
	ds_bpermute_b32 v11, v7, v5
	v_xor_b32_e32 v8, 4, v1
	v_cmp_lt_i32_e32 vcc, v8, v9
	s_waitcnt lgkmcnt(0)
	v_max_f32_e32 v11, v11, v11
	v_cndmask_b32_e32 v8, v1, v8, vcc
	v_lshlrev_b32_e32 v8, 2, v8
	v_max_f32_e32 v5, v5, v11
	ds_bpermute_b32 v11, v8, v5
	v_cmp_lt_i32_e32 vcc, v20, v9
	s_nop 1
	v_cndmask_b32_e32 v1, v1, v20, vcc
	v_lshlrev_b32_e32 v9, 2, v1
	s_waitcnt lgkmcnt(0)
	v_max_f32_e32 v1, v11, v11
	v_max_f32_e32 v11, v5, v1
	ds_bpermute_b32 v20, v9, v11
	v_mov_b32_e32 v1, 0x8000
	v_mov_b32_e32 v5, 0x800000
	s_waitcnt lgkmcnt(0)
	v_max_f32_e32 v10, v20, v20
	v_max_f32_e32 v10, v11, v10
	v_div_scale_f32 v11, s[14:15], v10, v10, s3
	v_rcp_f32_e32 v22, v11
	v_div_scale_f32 v23, vcc, s3, v10, s3
	v_lshl_add_u64 v[20:21], s[8:9], 0, v[2:3]
	v_fma_f32 v24, -v11, v22, 1.0
	v_fmac_f32_e32 v22, v24, v22
	v_mul_f32_e32 v24, v23, v22
	v_fma_f32 v25, -v11, v24, v23
	v_fmac_f32_e32 v24, v25, v22
	v_fma_f32 v11, -v11, v24, v23
	v_div_fmas_f32 v11, v11, v22, v24
	v_div_fixup_f32 v11, v11, v10, s3
	v_cmp_lt_f32_e32 vcc, 0, v10
	s_nop 1
	v_cndmask_b32_e32 v11, 0, v11, vcc
	v_mul_f32_e32 v12, v12, v11
	v_mul_f32_e32 v16, v16, v11
	v_mul_f32_e32 v13, v13, v11
	v_mul_f32_e32 v17, v17, v11
	v_mul_f32_e32 v14, v14, v11
	v_mul_f32_e32 v18, v18, v11
	v_rndne_f32_e32 v12, v12
	v_rndne_f32_e32 v16, v16
	v_rndne_f32_e32 v13, v13
	v_rndne_f32_e32 v17, v17
	v_mul_f32_e32 v15, v15, v11
	v_mul_f32_e32 v11, v19, v11
	v_rndne_f32_e32 v14, v14
	v_rndne_f32_e32 v18, v18
	v_cvt_i32_f32_e32 v12, v12
	v_cvt_i32_f32_e32 v16, v16
	v_cvt_i32_f32_e32 v13, v13
	v_cvt_i32_f32_e32 v17, v17
	v_rndne_f32_e32 v15, v15
	v_rndne_f32_e32 v11, v11
	v_cvt_i32_f32_e32 v14, v14
	v_cvt_i32_f32_e32 v18, v18
	v_cvt_i32_f32_sdwa v15, v15 dst_sel:BYTE_3 dst_unused:UNUSED_PAD src0_sel:DWORD
	v_cvt_i32_f32_sdwa v11, v11 dst_sel:BYTE_3 dst_unused:UNUSED_PAD src0_sel:DWORD
	v_add_u32_e32 v16, 0x80, v16
	v_add_u32_e32 v12, 0x80, v12
	v_lshl_add_u32 v17, v17, 8, v1
	v_lshl_add_u32 v13, v13, 8, v1
	v_lshl_add_u32 v18, v18, 16, v5
	v_lshl_add_u32 v14, v14, 16, v5
	v_or_b32_e32 v16, v17, v16
	v_or_b32_e32 v12, v13, v12
	v_xor_b32_e32 v11, 0x80000000, v11
	v_xor_b32_e32 v15, 0x80000000, v15
	v_or_b32_e32 v13, v16, v18
	v_or_b32_e32 v12, v12, v14
	v_or_b32_e32 v13, v13, v11
	v_or_b32_e32 v12, v12, v15
	v_mov_b32_e32 v28, v12
	v_mov_b32_e32 v29, v13
	s_nop 1
	v_mov_b32_dpp v30, v12 quad_perm:[1,1,3,3] row_mask:0xf bank_mask:0xf
	v_mov_b32_dpp v31, v13 quad_perm:[1,1,3,3] row_mask:0xf bank_mask:0xf
	s_mov_b64 s[20:21], exec
	s_mov_b32 s22, 0x55555555
	s_mov_b32 s23, 0x55555555
	s_and_b64 exec, exec, s[22:23]
	global_store_dwordx4 v[20:21], v[28:31], off sc1
	s_mov_b64 exec, s[20:21]
	s_and_saveexec_b64 s[14:15], s[4:5]
	s_cbranch_execz .LBB0_18
	s_mov_b32 s16, 0x3c010204
	v_lshrrev_b64 v[2:3], 6, v[2:3]
	v_fma_mixlo_f16 v10, v10, s16, 0
	v_lshl_add_u64 v[2:3], s[6:7], 0, v[2:3]
	global_store_short v[2:3], v10, off
.LBB0_18:
	s_or_b64 exec, exec, s[14:15]
	s_or_b32 s12, s12, 1
	s_lshl_b64 s[12:13], s[12:13], 13
	v_mov_b32_e32 v3, s13
	v_or_b32_e32 v2, s12, v4
	v_lshl_add_u64 v[18:19], v[2:3], 2, s[10:11]
	global_load_dwordx4 v[10:13], v[18:19], off
	global_load_dwordx4 v[14:17], v[18:19], off offset:16
	s_waitcnt vmcnt(1)
	v_max3_f32 v4, |v10|, 0, |v11|
	v_max3_f32 v4, v4, |v12|, |v13|
	s_waitcnt vmcnt(0)
	v_max3_f32 v4, v4, |v14|, |v15|
	v_max3_f32 v4, v4, |v16|, |v17|
	ds_bpermute_b32 v6, v6, v4
	s_waitcnt lgkmcnt(0)
	v_max_f32_e32 v6, v6, v6
	v_max_f32_e32 v4, v4, v6
	ds_bpermute_b32 v6, v7, v4
	s_waitcnt lgkmcnt(0)
	v_max_f32_e32 v6, v6, v6
	v_max_f32_e32 v4, v4, v6
	ds_bpermute_b32 v6, v8, v4
	s_waitcnt lgkmcnt(0)
	v_max_f32_e32 v6, v6, v6
	v_max_f32_e32 v4, v4, v6
	ds_bpermute_b32 v6, v9, v4
	s_waitcnt lgkmcnt(0)
	v_max_f32_e32 v6, v6, v6
	v_max_f32_e32 v4, v4, v6
	v_div_scale_f32 v8, s[10:11], v4, v4, s3
	v_rcp_f32_e32 v9, v8
	v_div_scale_f32 v18, vcc, s3, v4, s3
	v_lshl_add_u64 v[6:7], s[8:9], 0, v[2:3]
	v_fma_f32 v19, -v8, v9, 1.0
	v_fmac_f32_e32 v9, v19, v9
	v_mul_f32_e32 v19, v18, v9
	v_fma_f32 v20, -v8, v19, v18
	v_fmac_f32_e32 v19, v20, v9
	v_fma_f32 v8, -v8, v19, v18
	v_div_fmas_f32 v8, v8, v9, v19
	v_div_fixup_f32 v8, v8, v4, s3
	v_cmp_lt_f32_e32 vcc, 0, v4
	s_nop 1
	v_cndmask_b32_e32 v8, 0, v8, vcc
	v_mul_f32_e32 v9, v10, v8
	v_mul_f32_e32 v10, v14, v8
	v_mul_f32_e32 v11, v11, v8
	v_mul_f32_e32 v14, v15, v8
	v_mul_f32_e32 v12, v12, v8
	v_mul_f32_e32 v15, v16, v8
	v_rndne_f32_e32 v9, v9
	v_rndne_f32_e32 v10, v10
	v_rndne_f32_e32 v11, v11
	v_rndne_f32_e32 v14, v14
	v_mul_f32_e32 v13, v13, v8
	v_mul_f32_e32 v8, v17, v8
	v_rndne_f32_e32 v12, v12
	v_rndne_f32_e32 v15, v15
	v_cvt_i32_f32_e32 v9, v9
	v_cvt_i32_f32_e32 v10, v10
	v_cvt_i32_f32_e32 v11, v11
	v_cvt_i32_f32_e32 v14, v14
	v_rndne_f32_e32 v13, v13
	v_rndne_f32_e32 v8, v8
	v_cvt_i32_f32_e32 v12, v12
	v_cvt_i32_f32_e32 v15, v15
	v_cvt_i32_f32_sdwa v13, v13 dst_sel:BYTE_3 dst_unused:UNUSED_PAD src0_sel:DWORD
	v_cvt_i32_f32_sdwa v8, v8 dst_sel:BYTE_3 dst_unused:UNUSED_PAD src0_sel:DWORD
	v_add_u32_e32 v10, 0x80, v10
	v_add_u32_e32 v9, 0x80, v9
	v_lshl_add_u32 v14, v14, 8, v1
	v_lshl_add_u32 v1, v11, 8, v1
	v_lshl_add_u32 v11, v15, 16, v5
	v_lshl_add_u32 v5, v12, 16, v5
	v_or_b32_e32 v10, v14, v10
	v_or_b32_e32 v1, v1, v9
	v_xor_b32_e32 v8, 0x80000000, v8
	v_xor_b32_e32 v12, 0x80000000, v13
	v_or_b32_e32 v9, v10, v11
	v_or_b32_e32 v1, v1, v5
	v_or_b32_e32 v9, v9, v8
	v_or_b32_e32 v8, v1, v12
	v_mov_b32_e32 v28, v8
	v_mov_b32_e32 v29, v9
	s_nop 1
	v_mov_b32_dpp v30, v8 quad_perm:[1,1,3,3] row_mask:0xf bank_mask:0xf
	v_mov_b32_dpp v31, v9 quad_perm:[1,1,3,3] row_mask:0xf bank_mask:0xf
	s_mov_b64 s[20:21], exec
	s_mov_b32 s22, 0x55555555
	s_mov_b32 s23, 0x55555555
	s_and_b64 exec, exec, s[22:23]
	global_store_dwordx4 v[6:7], v[28:31], off sc1
	s_mov_b64 exec, s[20:21]
	s_and_saveexec_b64 s[8:9], s[4:5]
	s_cbranch_execz .LBB0_20
	s_mov_b32 s3, 0x3c010204
	v_lshrrev_b64 v[2:3], 6, v[2:3]
	v_fma_mixlo_f16 v1, v4, s3, 0
	v_lshl_add_u64 v[2:3], s[6:7], 0, v[2:3]
	global_store_short v[2:3], v1, off

	.amdhsa_kernel _Z12sort1_kernelPKfPKiS0_S0_S0_S0_PDF16_S3_S3_S3_PiPjPhS3_S3_
		.amdhsa_group_segment_fixed_size 14560
		.amdhsa_private_segment_fixed_size 0
		.amdhsa_kernarg_size 120
		.amdhsa_user_sgpr_count 2
		.amdhsa_user_sgpr_dispatch_ptr 0
		.amdhsa_user_sgpr_queue_ptr 0
		.amdhsa_user_sgpr_kernarg_segment_ptr 1
		.amdhsa_user_sgpr_dispatch_id 0
		.amdhsa_user_sgpr_kernarg_preload_length 0
		.amdhsa_user_sgpr_kernarg_preload_offset 0
		.amdhsa_user_sgpr_private_segment_size 0
		.amdhsa_uses_dynamic_stack 0
		.amdhsa_enable_private_segment 0
		.amdhsa_system_sgpr_workgroup_id_x 1
		.amdhsa_system_sgpr_workgroup_id_y 0
		.amdhsa_system_sgpr_workgroup_id_z 0
		.amdhsa_system_sgpr_workgroup_info 0
		.amdhsa_system_vgpr_workitem_id 0
		.amdhsa_next_free_vgpr 32
		.amdhsa_next_free_sgpr 24
		.amdhsa_accum_offset 32
		.amdhsa_reserve_vcc 1
		.amdhsa_float_round_mode_32 0
		.amdhsa_float_round_mode_16_64 0
		.amdhsa_float_denorm_mode_32 3
		.amdhsa_float_denorm_mode_16_64 3
		.amdhsa_dx10_clamp 1
		.amdhsa_ieee_mode 1
		.amdhsa_fp16_overflow 0
		.amdhsa_tg_split 0
		.amdhsa_exception_fp_ieee_invalid_op 0
		.amdhsa_exception_fp_denorm_src 0
		.amdhsa_exception_fp_ieee_div_zero 0
		.amdhsa_exception_fp_ieee_overflow 0
		.amdhsa_exception_fp_ieee_underflow 0
		.amdhsa_exception_fp_ieee_inexact 0
		.amdhsa_exception_int_div_zero 0
	.end_amdhsa_kernel

amdhsa.kernels:
  - .agpr_count:     0
    .args:
      - .actual_access:  read_only
        .address_space:  global
        .offset:         0
        .size:           8
        .value_kind:     global_buffer
      - .actual_access:  read_only
        .address_space:  global
        .offset:         8
        .size:           8
        .value_kind:     global_buffer
      - .actual_access:  read_only
        .address_space:  global
        .offset:         16
        .size:           8
        .value_kind:     global_buffer
      - .actual_access:  read_only
        .address_space:  global
        .offset:         24
        .size:           8
        .value_kind:     global_buffer
      - .actual_access:  read_only
        .address_space:  global
        .offset:         32
        .size:           8
        .value_kind:     global_buffer
      - .actual_access:  read_only
        .address_space:  global
        .offset:         40
        .size:           8
        .value_kind:     global_buffer
      - .actual_access:  read_only
        .address_space:  global
        .offset:         48
        .size:           8
        .value_kind:     global_buffer
      - .actual_access:  read_only
        .address_space:  global
        .offset:         56
        .size:           8
        .value_kind:     global_buffer
      - .actual_access:  write_only
        .address_space:  global
        .offset:         64
        .size:           8
        .value_kind:     global_buffer
      - .actual_access:  write_only
        .address_space:  global
        .offset:         72
        .size:           8
        .value_kind:     global_buffer
      - .actual_access:  write_only
        .address_space:  global
        .offset:         80
        .size:           8
        .value_kind:     global_buffer
      - .actual_access:  write_only
        .address_space:  global
        .offset:         88
        .size:           8
        .value_kind:     global_buffer
      - .actual_access:  write_only
        .address_space:  global
        .offset:         96
        .size:           8
        .value_kind:     global_buffer
      - .actual_access:  write_only
        .address_space:  global
        .offset:         104
        .size:           8
        .value_kind:     global_buffer
      - .actual_access:  write_only
        .address_space:  global
        .offset:         112
        .size:           8
        .value_kind:     global_buffer
    .group_segment_fixed_size: 14560
    .kernarg_segment_align: 8
    .kernarg_segment_size: 120
    .language:       OpenCL C
    .language_version:
      - 2
      - 0
    .max_flat_workgroup_size: 1024
    .name:           _Z12sort1_kernelPKfPKiS0_S0_S0_S0_PDF16_S3_S3_S3_PiPjPhS3_S3_
    .private_segment_fixed_size: 0
    .sgpr_count:     30
    .sgpr_spill_count: 0
    .symbol:         _Z12sort1_kernelPKfPKiS0_S0_S0_S0_PDF16_S3_S3_S3_PiPjPhS3_S3_.kd
    .uniform_work_group_size: 1
    .uses_dynamic_stack: false
    .vgpr_count:     32
    .vgpr_spill_count: 0
    .wavefront_size: 64
  - .agpr_count:     0
    .args:
      - .actual_access:  read_only
        .address_space:  global
        .offset:         0
        .size:           8
        .value_kind:     global_buffer
      - .actual_access:  read_only
        .address_space:  global
        .offset:         8
        .size:           8
        .value_kind:     global_buffer
      - .actual_access:  write_only
        .address_space:  global
        .offset:         16
        .size:           8
        .value_kind:     global_buffer
      - .actual_access:  write_only
        .address_space:  global
        .offset:         24
        .size:           8
        .value_kind:     global_buffer
      - .actual_access:  read_only
        .address_space:  global
        .offset:         32
        .size:           8
        .value_kind:     global_buffer
      - .actual_access:  read_only
        .address_space:  global
        .offset:         40
        .size:           8
        .value_kind:     global_buffer
      - .actual_access:  write_only
        .address_space:  global
        .offset:         48
        .size:           8
        .value_kind:     global_buffer
      - .actual_access:  write_only
        .address_space:  global
        .offset:         56
        .size:           8
        .value_kind:     global_buffer
      - .actual_access:  write_only
        .address_space:  global
        .offset:         64
        .size:           8
        .value_kind:     global_buffer
    .group_segment_fixed_size: 21792
    .kernarg_segment_align: 8
    .kernarg_segment_size: 72
    .language:       OpenCL C
    .language_version:
      - 2
      - 0
    .max_flat_workgroup_size: 1024
    .name:           _Z12sort2_kernelPKfPDF16_PhS1_PKiPKjP15HIP_vector_typeIiLj4EEPiPt
    .private_segment_fixed_size: 0
    .sgpr_count:     48
    .sgpr_spill_count: 0
    .symbol:         _Z12sort2_kernelPKfPDF16_PhS1_PKiPKjP15HIP_vector_typeIiLj4EEPiPt.kd
    .uniform_work_group_size: 1
    .uses_dynamic_stack: false
    .vgpr_count:     33
    .vgpr_spill_count: 0
    .wavefront_size: 64
  - .agpr_count:     0
    .args:
      - .actual_access:  read_only
        .address_space:  global
        .offset:         0
        .size:           8
        .value_kind:     global_buffer
      - .actual_access:  read_only
        .address_space:  global
        .offset:         8
        .size:           8
        .value_kind:     global_buffer
      - .actual_access:  read_only
        .address_space:  global
        .offset:         16
        .size:           8
        .value_kind:     global_buffer
      - .actual_access:  read_only
        .address_space:  global
        .offset:         24
        .size:           8
        .value_kind:     global_buffer
      - .actual_access:  read_only
        .address_space:  global
        .offset:         32
        .size:           8
        .value_kind:     global_buffer
      - .actual_access:  read_only
        .address_space:  global
        .offset:         40
        .size:           8
        .value_kind:     global_buffer
      - .actual_access:  read_only
        .address_space:  global
        .offset:         48
        .size:           8
        .value_kind:     global_buffer
      - .actual_access:  read_only
        .address_space:  global
        .offset:         56
        .size:           8
        .value_kind:     global_buffer
      - .actual_access:  read_only
        .address_space:  global
        .offset:         64
        .size:           8
        .value_kind:     global_buffer
      - .actual_access:  write_only
        .address_space:  global
        .offset:         72
        .size:           8
        .value_kind:     global_buffer
      - .actual_access:  write_only
        .address_space:  global
        .offset:         80
        .size:           8
        .value_kind:     global_buffer
      - .actual_access:  write_only
        .address_space:  global
        .offset:         88
        .size:           8
        .value_kind:     global_buffer
    .group_segment_fixed_size: 0
    .kernarg_segment_align: 8
    .kernarg_segment_size: 96
    .language:       OpenCL C
    .language_version:
      - 2
      - 0
    .max_flat_workgroup_size: 1024
    .name:           _Z12layer_kernelILb1ELi128EEvPKfPKDF16_PKhS3_PK15HIP_vector_typeIiLj4EEPKtPKiS3_S1_PvPhPDF16_
    .private_segment_fixed_size: 0
    .sgpr_count:     70
    .sgpr_spill_count: 0
    .symbol:         _Z12layer_kernelILb1ELi128EEvPKfPKDF16_PKhS3_PK15HIP_vector_typeIiLj4EEPKtPKiS3_S1_PvPhPDF16_.kd
    .uniform_work_group_size: 1
    .uses_dynamic_stack: false
    .vgpr_count:     128
    .vgpr_spill_count: 0
    .wavefront_size: 64
  - .agpr_count:     0
    .args:
      - .actual_access:  read_only
        .address_space:  global
        .offset:         0
        .size:           8
        .value_kind:     global_buffer
      - .actual_access:  read_only
        .address_space:  global
        .offset:         8
        .size:           8
        .value_kind:     global_buffer
      - .actual_access:  read_only
        .address_space:  global
        .offset:         16
        .size:           8
        .value_kind:     global_buffer
      - .actual_access:  read_only
        .address_space:  global
        .offset:         24
        .size:           8
        .value_kind:     global_buffer
      - .actual_access:  read_only
        .address_space:  global
        .offset:         32
        .size:           8
        .value_kind:     global_buffer
      - .actual_access:  read_only
        .address_space:  global
        .offset:         40
        .size:           8
        .value_kind:     global_buffer
      - .actual_access:  read_only
        .address_space:  global
        .offset:         48
        .size:           8
        .value_kind:     global_buffer
      - .actual_access:  read_only
        .address_space:  global
        .offset:         56
        .size:           8
        .value_kind:     global_buffer
      - .actual_access:  read_only
        .address_space:  global
        .offset:         64
        .size:           8
        .value_kind:     global_buffer
      - .actual_access:  write_only
        .address_space:  global
        .offset:         72
        .size:           8
        .value_kind:     global_buffer
      - .actual_access:  read_only
        .address_space:  global
        .offset:         80
        .size:           8
        .value_kind:     global_buffer
      - .actual_access:  read_only
        .address_space:  global
        .offset:         88
        .size:           8
        .value_kind:     global_buffer
    .group_segment_fixed_size: 0
    .kernarg_segment_align: 8
    .kernarg_segment_size: 96
    .language:       OpenCL C
    .language_version:
      - 2
      - 0
    .max_flat_workgroup_size: 1024
    .name:           _Z12layer_kernelILb0ELi0EEvPKfPKDF16_PKhS3_PK15HIP_vector_typeIiLj4EEPKtPKiS3_S1_PvPhPDF16_
    .private_segment_fixed_size: 0
    .sgpr_count:     70
    .sgpr_spill_count: 0
    .symbol:         _Z12layer_kernelILb0ELi0EEvPKfPKDF16_PKhS3_PK15HIP_vector_typeIiLj4EEPKtPKiS3_S1_PvPhPDF16_.kd
    .uniform_work_group_size: 1
    .uses_dynamic_stack: false
    .vgpr_count:     128
    .vgpr_spill_count: 0
    .wavefront_size: 64
